# hybrid K1 (ring 16, 14 private chunks + contiguous pool) + one-lane address-translation touch 64KiB ahead of each requested chunk
# baseline (speedup 1.0000x reference)
.Lk1_haveid:
	s_mul_i32 s57, s57, 0x4000
	s_lshr_b32 s58, s57, 2
	s_add_u32 s6, s4, s57
	s_addc_u32 s7, s5, 0
	s_add_u32 s61, s57, 0x10000
	s_cmp_lt_u32 s61, 0x23ffffc0
	s_cbranch_scc0 .Lk1_nopf
	s_add_u32 s62, s4, s61
	s_addc_u32 s63, s5, 0
	s_mov_b64 exec, 1
	global_load_dword v7, v27, s[62:63]
	s_mov_b64 exec, -1
.Lk1_nopf:
	s_add_u32 s60, s26, 3
	s_cmp_lt_u32 s60, 14
	s_cbranch_scc1 .Lk1_noreq
	s_mov_b64 exec, 1
	global_atomic_add v26, v27, v21, s[54:55] sc0
	s_mov_b64 exec, -1
